# speedup vs baseline: 1.0015x; 1.0015x over previous
.LBB2_6:
	s_or_b64 exec, exec, s[18:19]
	v_xor_b32_e32 v23, 32, v23
	s_add_i32 s38, 0, 0x1c000
	v_lshlrev_b32_e32 v23, 2, v23
	v_lshlrev_b32_e32 v199, 2, v25
	s_waitcnt vmcnt(4) lgkmcnt(0)
	s_barrier
	v_add3_u32 v23, s38, v23, v199
	ds_read_b32 v23, v23
	v_max_f32_e32 v24, v24, v24
	v_mul_f32_e32 v22, 0x3db8aa3b, v22
	v_mov_b32_e32 v164, 0
	v_mov_b32_e32 v165, 0
	s_waitcnt lgkmcnt(0)
	s_movk_i32 s45, 0x4000
	v_add3_u32 v250, s45, v184, v185
	v_add3_u32 v251, s45, v184, v186
	v_add3_u32 v252, s45, v184, v187
	v_add3_u32 v253, s45, v184, v188
	ds_read_b128 v[218:221], v250 offset:49152
	ds_read_b128 v[222:225], v251 offset:49152
	ds_read_b128 v[242:245], v252 offset:49152
	ds_read_b128 v[246:249], v253 offset:49152
	v_add3_u32 v250, s45, v184, v189
	v_add3_u32 v251, s45, v184, v190
	v_add3_u32 v252, s45, v184, v191
	v_add3_u32 v253, s45, v184, v192
	ds_read_b128 v[202:205], v250 offset:49152
	ds_read_b128 v[206:209], v251 offset:49152
	ds_read_b128 v[210:213], v252 offset:49152
	ds_read_b128 v[214:217], v253 offset:49152
	v_max_f32_e32 v23, v23, v23
	v_max_f32_e32 v197, v24, v23
	v_mov_b32_e32 v23, 2.0
	v_fmamk_f32 v200, v197, 0xbdb8aa3b, v23
	v_fmamk_f32 v23, v22, 0xcb400000, v200
	v_fma_f32 v2, v2, v22, v23
	v_fma_f32 v3, v3, v22, v23
	v_fma_f32 v6, v6, v22, v23
	v_fma_f32 v7, v7, v22, v23
	v_fma_f32 v10, v10, v22, v23
	v_fma_f32 v11, v11, v22, v23
	v_fma_f32 v14, v14, v22, v23
	v_fma_f32 v15, v15, v22, v23
	v_exp_f32_e32 v2, v2
	v_exp_f32_e32 v3, v3
	v_exp_f32_e32 v6, v6
	v_exp_f32_e32 v7, v7
	v_exp_f32_e32 v10, v10
	v_exp_f32_e32 v11, v11
	v_exp_f32_e32 v14, v14
	v_exp_f32_e32 v15, v15
	v_fma_f32 v4, v4, v22, v23
	v_fma_f32 v5, v5, v22, v23
	v_fma_f32 v8, v8, v22, v23
	v_fma_f32 v9, v9, v22, v23
	v_fma_f32 v12, v12, v22, v23
	v_fma_f32 v13, v13, v22, v23
	v_fma_f32 v16, v16, v22, v23
	v_fmac_f32_e32 v23, v17, v22
	v_mov_b32_e32 v166, 0
	v_mov_b32_e32 v167, 0
	v_exp_f32_e32 v4, v4
	v_exp_f32_e32 v5, v5
	v_exp_f32_e32 v8, v8
	v_exp_f32_e32 v9, v9
	v_exp_f32_e32 v12, v12
	v_exp_f32_e32 v13, v13
	v_exp_f32_e32 v16, v16
	v_exp_f32_e32 v17, v23
	v_add_f32_e32 v250, v2, v3
	v_add_f32_e32 v251, v4, v5
	v_add_f32_e32 v252, v6, v7
	v_add_f32_e32 v253, v8, v9
	v_add_f32_e32 v250, v250, v251
	v_add_f32_e32 v252, v252, v253
	v_add_f32_e32 v251, v10, v11
	v_add_f32_e32 v253, v12, v13
	v_add_f32_e32 v250, v250, v252
	v_add_f32_e32 v251, v251, v253
	v_add_f32_e32 v252, v14, v15
	v_add_f32_e32 v253, v16, v17
	v_add_f32_e32 v250, v250, v251
	v_add_f32_e32 v252, v252, v253
	v_add_f32_e32 v250, v250, v252
	v_cvt_pk_fp8_f32 v164, v2, v3
	v_cvt_pk_fp8_f32 v165, v6, v7
	v_cvt_pk_fp8_f32 v166, v10, v11
	v_cvt_pk_fp8_f32 v167, v14, v15
	s_lshl_b32 s0, s22, 11
	s_add_i32 s0, s0, 0
	s_add_i32 s0, s0, 0x18000
	v_cvt_pk_fp8_f32 v164, v4, v5 op_sel:[0,0,1]
	v_cvt_pk_fp8_f32 v165, v8, v9 op_sel:[0,0,1]
	v_cvt_pk_fp8_f32 v166, v12, v13 op_sel:[0,0,1]
	v_cvt_pk_fp8_f32 v167, v16, v17 op_sel:[0,0,1]
	v_lshl_add_u32 v193, v198, 4, s0
	v_lshrrev_b32_e32 v3, 2, v0
	v_lshlrev_b32_e32 v6, 1, v183
	s_lshl_b32 s0, s20, 20
	v_bfe_u32 v4, v0, 2, 2
	v_lshl_or_b32 v5, v1, 6, s24
	v_bitop3_b32 v3, v6, v3, 3 bitop3:0x78
	s_or_b32 s18, s0, s23
	v_lshl_add_u32 v194, s34, 10, v193
	v_lshl_or_b32 v195, v3, 4, v5
	v_bitop3_b32 v3, v6, v4, 1 bitop3:0x36
	v_add3_u32 v4, s21, v20, v21
	s_add_u32 s0, s6, s18
	ds_write_b128 v194, v[164:167]
	v_lshl_or_b32 v196, v3, 4, v5
	v_ashrrev_i32_e32 v5, 31, v4
	s_addc_u32 s1, s7, 0
	s_waitcnt vmcnt(2) lgkmcnt(0)
	s_barrier
	s_mov_b64 s[60:61], s[0:1]
	v_lshl_add_u64 v[170:171], s[0:1], 0, v[4:5]
	v_add3_u32 v4, s21, v18, v19
	s_add_u32 s0, s8, s18
	v_mov_b32_e32 v2, 0
	v_ashrrev_i32_e32 v5, 31, v4
	s_addc_u32 s1, s9, 0
	s_mov_b32 s39, 0
	s_mov_b32 s40, 1
	s_mov_b64 s[64:65], s[0:1]
	v_lshl_add_u64 v[172:173], s[0:1], 0, v[4:5]
	s_mov_b64 s[6:7], 0
	s_movk_i32 s41, 0x2000
	s_mov_b64 s[8:9], 0xc000
	s_mov_b64 s[18:19], 0xe000
	s_mov_b64 s[20:21], 0x8000
	s_mov_b64 s[22:23], 0xa000
	s_mov_b32 s42, 0x42966666
	v_mov_b32_e32 v82, 0x4b400000
	v_mov_b32_e32 v100, 0x38383838
	s_mov_b32 s0, 0
	s_mov_b32 s43, 1
	v_mov_b32_e32 v3, v2
	v_mov_b32_e32 v4, v2
	v_mov_b32_e32 v5, v2
	v_mov_b32_e32 v6, v2
	v_mov_b32_e32 v7, v2
	v_mov_b32_e32 v8, v2
	v_mov_b32_e32 v9, v2
	v_mov_b32_e32 v10, v2
	v_mov_b32_e32 v11, v2
	v_mov_b32_e32 v12, v2
	v_mov_b32_e32 v13, v2
	v_mov_b32_e32 v14, v2
	v_mov_b32_e32 v15, v2
	v_mov_b32_e32 v16, v2
	v_mov_b32_e32 v17, v2
	v_mov_b32_e32 v18, v2
	v_mov_b32_e32 v19, v2
	v_mov_b32_e32 v20, v2
	v_mov_b32_e32 v21, v2
	v_mov_b32_e32 v22, v2
	v_mov_b32_e32 v23, v2
	v_mov_b32_e32 v24, v2
	v_mov_b32_e32 v25, v2
	v_mov_b32_e32 v26, v2
	v_mov_b32_e32 v27, v2
	v_mov_b32_e32 v28, v2
	v_mov_b32_e32 v29, v2
	v_mov_b32_e32 v30, v2
	v_mov_b32_e32 v31, v2
	v_mov_b32_e32 v32, v2
	v_mov_b32_e32 v33, v2
	v_mov_b32_e32 v34, v2
	v_mov_b32_e32 v35, v2
	v_mov_b32_e32 v36, v2
	v_mov_b32_e32 v37, v2
	v_mov_b32_e32 v38, v2
	v_mov_b32_e32 v39, v2
	v_mov_b32_e32 v40, v2
	v_mov_b32_e32 v41, v2
	v_mov_b32_e32 v42, v2
	v_mov_b32_e32 v43, v2
	v_mov_b32_e32 v44, v2
	v_mov_b32_e32 v45, v2
	v_mov_b32_e32 v46, v2
	v_mov_b32_e32 v47, v2
	v_mov_b32_e32 v48, v2
	v_mov_b32_e32 v49, v2
	v_mov_b32_e32 v50, v2
	v_mov_b32_e32 v51, v2
	v_mov_b32_e32 v52, v2
	v_mov_b32_e32 v53, v2
	v_mov_b32_e32 v54, v2
	v_mov_b32_e32 v55, v2
	v_mov_b32_e32 v56, v2
	v_mov_b32_e32 v57, v2
	v_mov_b32_e32 v58, v2
	v_mov_b32_e32 v59, v2
	v_mov_b32_e32 v60, v2
	v_mov_b32_e32 v61, v2
	v_mov_b32_e32 v62, v2
	v_mov_b32_e32 v63, v2
	v_mov_b32_e32 v64, v2
	v_mov_b32_e32 v65, v2
	v_mov_b32_e32 v66, v2
	v_mov_b32_e32 v67, v2
	v_mov_b32_e32 v68, v2
	v_mov_b32_e32 v69, v2
	v_mov_b32_e32 v70, v2
	v_mov_b32_e32 v71, v2
	v_mov_b32_e32 v72, v2
	v_mov_b32_e32 v73, v2
	v_mov_b32_e32 v74, v2
	v_mov_b32_e32 v75, v2
	v_mov_b32_e32 v76, v2
	v_mov_b32_e32 v77, v2
	v_mov_b32_e32 v78, v2
	v_mov_b32_e32 v79, v2
	v_mov_b32_e32 v80, v2
	v_mov_b32_e32 v81, v2
	v_mov_b32_e32 v66, v250
	v_mov_b32_e32 v226, 0x4b400000
	v_mov_b32_e32 v227, v226
	v_mov_b32_e32 v228, v226
	v_mov_b32_e32 v229, v226
	v_mov_b32_e32 v230, v226
	v_mov_b32_e32 v231, v226
	v_mov_b32_e32 v232, v226
	v_mov_b32_e32 v233, v226
	v_mov_b32_e32 v234, v226
	v_mov_b32_e32 v235, v226
	v_mov_b32_e32 v236, v226
	v_mov_b32_e32 v237, v226
	v_mov_b32_e32 v238, v226
	v_mov_b32_e32 v239, v226
	v_mov_b32_e32 v240, v226
	v_mov_b32_e32 v241, v226
	v_add_u32_e32 v250, 0xc000, v184
	v_add_u32_e32 v185, v185, v250
	v_add_u32_e32 v186, v186, v250
	v_add_u32_e32 v187, v187, v250
	v_add_u32_e32 v188, v188, v250
	v_add_u32_e32 v189, v189, v250
	v_add_u32_e32 v190, v190, v250
	v_add_u32_e32 v191, v191, v250
	v_add_u32_e32 v192, v192, v250
	v_subrev_u32_e32 v252, s60, v170
	v_subrev_u32_e32 v255, s64, v172
	s_sub_u32 s1, s64, s60
	s_add_i32 s1, s1, 0xffffc000
	v_add_u32_e32 v254, 0x2000, v252
	v_add_u32_e32 v255, s1, v255
	v_add_u32_e32 v201, 0x2000, v255
	s_add_u32 s60, s60, 0xc000
	s_addc_u32 s61, s61, 0
	s_mov_b32 s42, 0x43dc0000
	s_mov_b64 s[54:55], -1
	v_mov_b32_e32 v108, v164
	v_mov_b32_e32 v109, v165
	v_mov_b32_e32 v110, v166
	v_mov_b32_e32 v111, v167
	v_lshlrev_b32_e32 v164, 1, v193
	v_sub_u32_e32 v164, v164, v194
	v_add_u32_e32 v164, 0x400, v164
	s_cmp_eq_u32 s34, 0
	s_cbranch_scc1 .Lat_nsw
	v_swap_b32 v195, v196
.Lat_nsw:
	v_mfma_i32_32x32x32_i8 v[84:99], v[218:221], v[132:135], v[226:241]
	v_mfma_i32_32x32x32_i8 v[84:99], v[222:225], v[136:139], v[84:99]
.Lat_u0:
	ds_read_b128 v[112:115], v164
	v_mfma_i32_32x32x32_i8 v[84:99], v[242:245], v[140:143], v[84:99]
	ds_read_b128 v[116:119], v195 offset:6144
	ds_read_b128 v[120:123], v196 offset:6144
	s_cmp_gt_u32 s43, 29
	s_cbranch_scc1 .Lat_nok0
	s_add_i32 m0, s31, 49152
	ds_read_b128 v[124:127], v195 offset:4096
	global_load_lds_dwordx4 v252, s[60:61]
	s_add_i32 m0, s31, 57344
	v_mfma_i32_32x32x32_i8 v[84:99], v[246:249], v[144:147], v[84:99]
	global_load_lds_dwordx4 v254, s[60:61]
	s_branch .Lat_k0

.Lat_v0:
	v_fma_f32 v86, v86, v250, v251
	v_fma_f32 v87, v87, v250, v251
	v_exp_f32_e32 v84, v84
	v_exp_f32_e32 v85, v85
	v_exp_f32_e32 v86, v86
	v_exp_f32_e32 v87, v87
	v_fma_f32 v88, v88, v250, v251
	v_fma_f32 v89, v89, v250, v251
	v_fma_f32 v90, v90, v250, v251
	v_fma_f32 v91, v91, v250, v251
	s_waitcnt lgkmcnt(8)
	v_mfma_f32_32x32x64_f8f6f4 v[18:33], v[108:115], v[124:131], v[18:33]
	v_add_f32_e32 v67, v84, v85
	v_add_f32_e32 v68, v86, v87
	v_exp_f32_e32 v88, v88
	v_exp_f32_e32 v89, v89
	v_exp_f32_e32 v90, v90
	v_exp_f32_e32 v91, v91
	v_add_f32_e32 v67, v67, v68
	v_cvt_pk_fp8_f32 v100, v84, v85
	v_cvt_pk_fp8_f32 v100, v86, v87 op_sel:[0,0,1]
	v_fma_f32 v92, v92, v250, v251
	v_fma_f32 v93, v93, v250, v251
	v_fma_f32 v94, v94, v250, v251
	v_fma_f32 v95, v95, v250, v251
	v_add_f32_e32 v68, v88, v89
	v_add_f32_e32 v69, v90, v91
	s_waitcnt lgkmcnt(6)
	v_mfma_f32_32x32x64_f8f6f4 v[50:65], v[108:115], v[202:209], v[50:65]
	ds_read_b128 v[202:205], v189 offset:32768
	ds_read_b128 v[206:209], v190 offset:32768
	v_exp_f32_e32 v92, v92
	v_exp_f32_e32 v93, v93
	v_exp_f32_e32 v94, v94
	v_exp_f32_e32 v95, v95
	v_add_f32_e32 v68, v68, v69
	v_cvt_pk_fp8_f32 v101, v88, v89
	v_cvt_pk_fp8_f32 v101, v90, v91 op_sel:[0,0,1]
	v_fma_f32 v96, v96, v250, v251
	v_fma_f32 v97, v97, v250, v251
	v_fma_f32 v98, v98, v250, v251
	v_fma_f32 v99, v99, v250, v251
	v_add_f32_e32 v67, v67, v68
	v_add_f32_e32 v68, v92, v93
	v_add_f32_e32 v69, v94, v95
	s_waitcnt lgkmcnt(6)
	v_mfma_f32_32x32x64_f8f6f4 v[34:49], v[108:115], v[210:217], v[34:49]
	ds_read_b128 v[210:213], v191 offset:32768
	ds_read_b128 v[214:217], v192 offset:32768
	v_exp_f32_e32 v96, v96
	v_exp_f32_e32 v97, v97
	v_exp_f32_e32 v98, v98
	v_exp_f32_e32 v99, v99
	v_add_f32_e32 v68, v68, v69
	v_cvt_pk_fp8_f32 v102, v92, v93
	v_cvt_pk_fp8_f32 v102, v94, v95 op_sel:[0,0,1]
	v_add_f32_e32 v67, v67, v68
	v_add_f32_e32 v68, v96, v97
	v_add_f32_e32 v69, v98, v99
	s_add_u32 s60, s60, 0x4000
	s_addc_u32 s61, s61, 0
	v_add_f32_e32 v68, v68, v69
	v_cvt_pk_fp8_f32 v103, v96, v97
	v_cvt_pk_fp8_f32 v103, v98, v99 op_sel:[0,0,1]
	v_add_f32_e32 v67, v67, v68
	ds_write_b128 v194, v[100:103] offset:8192
	v_cmp_ge_f32_e64 s[52:53], s42, v67
	v_add_f32_e32 v66, v66, v67
	s_add_i32 s43, s43, 1
	s_nop 0
	s_and_b64 s[54:55], s[54:55], s[52:53]
	s_cmp_eq_u32 s43, 32
	s_cbranch_scc1 .Lat_last
	s_waitcnt lgkmcnt(7)
	v_mfma_i32_32x32x32_i8 v[84:99], v[218:221], v[132:135], v[226:241]
	v_mfma_i32_32x32x32_i8 v[84:99], v[222:225], v[136:139], v[84:99]
	s_waitcnt vmcnt(2) lgkmcnt(0)
	s_barrier
.Lat_u1:
	ds_read_b128 v[104:107], v164 offset:8192
	v_mfma_i32_32x32x32_i8 v[84:99], v[242:245], v[140:143], v[84:99]
	ds_read_b128 v[116:119], v195 offset:22528
	ds_read_b128 v[120:123], v196 offset:22528
	s_add_i32 m0, s31, 65536
	ds_read_b128 v[124:127], v195 offset:20480
	global_load_lds_dwordx4 v252, s[60:61]
	s_add_i32 m0, s31, 73728
	v_mfma_i32_32x32x32_i8 v[84:99], v[246:249], v[144:147], v[84:99]
	global_load_lds_dwordx4 v254, s[60:61]
	ds_read_b128 v[128:131], v196 offset:20480
	v_mfma_i32_32x32x32_i8 v[84:99], v[202:205], v[148:151], v[84:99]
	ds_read_b128 v[202:205], v195 offset:16384
	v_mfma_i32_32x32x32_i8 v[84:99], v[206:209], v[152:155], v[84:99]
	ds_read_b128 v[206:209], v196 offset:16384
	v_mfma_i32_32x32x32_i8 v[84:99], v[210:213], v[156:159], v[84:99]
	ds_read_b128 v[210:213], v195 offset:18432
	v_mfma_i32_32x32x32_i8 v[84:99], v[214:217], v[160:163], v[84:99]
	ds_read_b128 v[214:217], v196 offset:18432
	v_readlane_b32 s50, v182, s43
	s_waitcnt lgkmcnt(6)
	v_mfma_f32_32x32x64_f8f6f4 v[2:17], v[100:107], v[116:123], v[2:17]
	ds_read_b128 v[218:221], v185
	ds_read_b128 v[222:225], v186
	ds_read_b128 v[242:245], v187
	ds_read_b128 v[246:249], v188
	v_mul_f32_e32 v82, s50, v168
	v_mul_f32_e32 v250, 0x3db8aa3b, v82
	v_fmamk_f32 v251, v250, 0xcb400000, v200
	s_mov_b32 m0, s31
	v_fma_f32 v84, v84, v250, v251
	global_load_lds_dwordx4 v255, s[60:61]
	s_add_i32 m0, s31, 8192
	v_fma_f32 v85, v85, v250, v251
	global_load_lds_dwordx4 v201, s[60:61]
	v_fma_f32 v86, v86, v250, v251
	v_fma_f32 v87, v87, v250, v251
	v_exp_f32_e32 v84, v84
	v_exp_f32_e32 v85, v85
	v_exp_f32_e32 v86, v86
	v_exp_f32_e32 v87, v87
	v_fma_f32 v88, v88, v250, v251
	v_fma_f32 v89, v89, v250, v251
	v_fma_f32 v90, v90, v250, v251
	v_fma_f32 v91, v91, v250, v251
	s_waitcnt lgkmcnt(8)
	v_mfma_f32_32x32x64_f8f6f4 v[18:33], v[100:107], v[124:131], v[18:33]
	v_add_f32_e32 v67, v84, v85
	v_add_f32_e32 v68, v86, v87
	v_exp_f32_e32 v88, v88
	v_exp_f32_e32 v89, v89
	v_exp_f32_e32 v90, v90
	v_exp_f32_e32 v91, v91
	v_add_f32_e32 v67, v67, v68
	v_cvt_pk_fp8_f32 v108, v84, v85
	v_cvt_pk_fp8_f32 v108, v86, v87 op_sel:[0,0,1]
	v_fma_f32 v92, v92, v250, v251
	v_fma_f32 v93, v93, v250, v251
	v_fma_f32 v94, v94, v250, v251
	v_fma_f32 v95, v95, v250, v251
	v_add_f32_e32 v68, v88, v89
	v_add_f32_e32 v69, v90, v91
	s_waitcnt lgkmcnt(6)
	v_mfma_f32_32x32x64_f8f6f4 v[50:65], v[100:107], v[202:209], v[50:65]
	ds_read_b128 v[202:205], v189
	ds_read_b128 v[206:209], v190
	v_exp_f32_e32 v92, v92
	v_exp_f32_e32 v93, v93
	v_exp_f32_e32 v94, v94
	v_exp_f32_e32 v95, v95
	v_add_f32_e32 v68, v68, v69
	v_cvt_pk_fp8_f32 v109, v88, v89
	v_cvt_pk_fp8_f32 v109, v90, v91 op_sel:[0,0,1]
	v_fma_f32 v96, v96, v250, v251
	v_fma_f32 v97, v97, v250, v251
	v_fma_f32 v98, v98, v250, v251
	v_fma_f32 v99, v99, v250, v251
	v_add_f32_e32 v67, v67, v68
	v_add_f32_e32 v68, v92, v93
	v_add_f32_e32 v69, v94, v95
	s_waitcnt lgkmcnt(6)
	v_mfma_f32_32x32x64_f8f6f4 v[34:49], v[100:107], v[210:217], v[34:49]
	ds_read_b128 v[210:213], v191
	ds_read_b128 v[214:217], v192
	v_exp_f32_e32 v96, v96
	v_exp_f32_e32 v97, v97
	v_exp_f32_e32 v98, v98
	v_exp_f32_e32 v99, v99
	v_add_f32_e32 v68, v68, v69
	v_cvt_pk_fp8_f32 v110, v92, v93
	v_cvt_pk_fp8_f32 v110, v94, v95 op_sel:[0,0,1]
	v_add_f32_e32 v67, v67, v68
	v_add_f32_e32 v68, v96, v97
	v_add_f32_e32 v69, v98, v99
	s_add_u32 s60, s60, 0x4000
	s_addc_u32 s61, s61, 0
	v_add_f32_e32 v68, v68, v69
	v_cvt_pk_fp8_f32 v111, v96, v97
	v_cvt_pk_fp8_f32 v111, v98, v99 op_sel:[0,0,1]
	v_add_f32_e32 v67, v67, v68
	ds_write_b128 v194, v[108:111]
	v_cmp_ge_f32_e64 s[52:53], s42, v67
	v_add_f32_e32 v66, v66, v67
	s_add_i32 s43, s43, 1
	s_nop 0
	s_and_b64 s[54:55], s[54:55], s[52:53]
	s_waitcnt lgkmcnt(7)
	v_mfma_i32_32x32x32_i8 v[84:99], v[218:221], v[132:135], v[226:241]
	v_mfma_i32_32x32x32_i8 v[84:99], v[222:225], v[136:139], v[84:99]
	s_waitcnt vmcnt(2) lgkmcnt(0)
	s_barrier
.Lat_u2:
	ds_read_b128 v[112:115], v164
	v_mfma_i32_32x32x32_i8 v[84:99], v[242:245], v[140:143], v[84:99]
	ds_read_b128 v[116:119], v195 offset:38912
	ds_read_b128 v[120:123], v196 offset:38912
	s_add_i32 m0, s31, 81920
	ds_read_b128 v[124:127], v195 offset:36864
	global_load_lds_dwordx4 v252, s[60:61]
	s_add_i32 m0, s31, 90112
	v_mfma_i32_32x32x32_i8 v[84:99], v[246:249], v[144:147], v[84:99]
	global_load_lds_dwordx4 v254, s[60:61]
	ds_read_b128 v[128:131], v196 offset:36864
	v_mfma_i32_32x32x32_i8 v[84:99], v[202:205], v[148:151], v[84:99]
	ds_read_b128 v[202:205], v195 offset:32768
	v_mfma_i32_32x32x32_i8 v[84:99], v[206:209], v[152:155], v[84:99]
	ds_read_b128 v[206:209], v196 offset:32768
	v_mfma_i32_32x32x32_i8 v[84:99], v[210:213], v[156:159], v[84:99]
	ds_read_b128 v[210:213], v195 offset:34816
	v_mfma_i32_32x32x32_i8 v[84:99], v[214:217], v[160:163], v[84:99]
	ds_read_b128 v[214:217], v196 offset:34816
	v_readlane_b32 s50, v182, s43
	s_waitcnt lgkmcnt(6)
	v_mfma_f32_32x32x64_f8f6f4 v[2:17], v[108:115], v[116:123], v[2:17]
	ds_read_b128 v[218:221], v185 offset:16384
	ds_read_b128 v[222:225], v186 offset:16384
	ds_read_b128 v[242:245], v187 offset:16384
	ds_read_b128 v[246:249], v188 offset:16384
	v_mul_f32_e32 v82, s50, v168
	v_mul_f32_e32 v250, 0x3db8aa3b, v82
	v_fmamk_f32 v251, v250, 0xcb400000, v200
	s_add_i32 m0, s31, 16384
	v_fma_f32 v84, v84, v250, v251
	global_load_lds_dwordx4 v255, s[60:61]
	s_add_i32 m0, s31, 24576
	v_fma_f32 v85, v85, v250, v251
	global_load_lds_dwordx4 v201, s[60:61]
	v_fma_f32 v86, v86, v250, v251
	v_fma_f32 v87, v87, v250, v251
	v_exp_f32_e32 v84, v84
	v_exp_f32_e32 v85, v85
	v_exp_f32_e32 v86, v86
	v_exp_f32_e32 v87, v87
	v_fma_f32 v88, v88, v250, v251
	v_fma_f32 v89, v89, v250, v251
	v_fma_f32 v90, v90, v250, v251
	v_fma_f32 v91, v91, v250, v251
	s_waitcnt lgkmcnt(8)
	v_mfma_f32_32x32x64_f8f6f4 v[18:33], v[108:115], v[124:131], v[18:33]
	v_add_f32_e32 v67, v84, v85
	v_add_f32_e32 v68, v86, v87
	v_exp_f32_e32 v88, v88
	v_exp_f32_e32 v89, v89
	v_exp_f32_e32 v90, v90
	v_exp_f32_e32 v91, v91
	v_add_f32_e32 v67, v67, v68
	v_cvt_pk_fp8_f32 v100, v84, v85
	v_cvt_pk_fp8_f32 v100, v86, v87 op_sel:[0,0,1]
	v_fma_f32 v92, v92, v250, v251
	v_fma_f32 v93, v93, v250, v251
	v_fma_f32 v94, v94, v250, v251
	v_fma_f32 v95, v95, v250, v251
	v_add_f32_e32 v68, v88, v89
	v_add_f32_e32 v69, v90, v91
	s_waitcnt lgkmcnt(6)
	v_mfma_f32_32x32x64_f8f6f4 v[50:65], v[108:115], v[202:209], v[50:65]
	ds_read_b128 v[202:205], v189 offset:16384
	ds_read_b128 v[206:209], v190 offset:16384
	v_exp_f32_e32 v92, v92
	v_exp_f32_e32 v93, v93
	v_exp_f32_e32 v94, v94
	v_exp_f32_e32 v95, v95
	v_add_f32_e32 v68, v68, v69
	v_cvt_pk_fp8_f32 v101, v88, v89
	v_cvt_pk_fp8_f32 v101, v90, v91 op_sel:[0,0,1]
	v_fma_f32 v96, v96, v250, v251
	v_fma_f32 v97, v97, v250, v251
	v_fma_f32 v98, v98, v250, v251
	v_fma_f32 v99, v99, v250, v251
	v_add_f32_e32 v67, v67, v68
	v_add_f32_e32 v68, v92, v93
	v_add_f32_e32 v69, v94, v95
	s_waitcnt lgkmcnt(6)
	v_mfma_f32_32x32x64_f8f6f4 v[34:49], v[108:115], v[210:217], v[34:49]
	ds_read_b128 v[210:213], v191 offset:16384
	ds_read_b128 v[214:217], v192 offset:16384
	v_exp_f32_e32 v96, v96
	v_exp_f32_e32 v97, v97
	v_exp_f32_e32 v98, v98
	v_exp_f32_e32 v99, v99
	v_add_f32_e32 v68, v68, v69
	v_cvt_pk_fp8_f32 v102, v92, v93
	v_cvt_pk_fp8_f32 v102, v94, v95 op_sel:[0,0,1]
	v_add_f32_e32 v67, v67, v68
	v_add_f32_e32 v68, v96, v97
	v_add_f32_e32 v69, v98, v99
	s_add_u32 s60, s60, 0x4000
	s_addc_u32 s61, s61, 0
	v_add_f32_e32 v68, v68, v69
	v_cvt_pk_fp8_f32 v103, v96, v97
	v_cvt_pk_fp8_f32 v103, v98, v99 op_sel:[0,0,1]
	v_add_f32_e32 v67, v67, v68
	ds_write_b128 v194, v[100:103] offset:8192
	v_cmp_ge_f32_e64 s[52:53], s42, v67
	v_add_f32_e32 v66, v66, v67
	s_add_i32 s43, s43, 1
	s_nop 0
	s_and_b64 s[54:55], s[54:55], s[52:53]
	s_waitcnt lgkmcnt(7)
	v_mfma_i32_32x32x32_i8 v[84:99], v[218:221], v[132:135], v[226:241]
	v_mfma_i32_32x32x32_i8 v[84:99], v[222:225], v[136:139], v[84:99]
	s_waitcnt vmcnt(2) lgkmcnt(0)
	s_barrier
.Lat_u3:
	ds_read_b128 v[104:107], v164 offset:8192
	v_mfma_i32_32x32x32_i8 v[84:99], v[242:245], v[140:143], v[84:99]
	ds_read_b128 v[116:119], v195 offset:6144
	ds_read_b128 v[120:123], v196 offset:6144
	s_add_i32 m0, s31, 49152
	ds_read_b128 v[124:127], v195 offset:4096
	global_load_lds_dwordx4 v252, s[60:61]
	s_add_i32 m0, s31, 57344
	v_mfma_i32_32x32x32_i8 v[84:99], v[246:249], v[144:147], v[84:99]
	global_load_lds_dwordx4 v254, s[60:61]
	ds_read_b128 v[128:131], v196 offset:4096
	v_mfma_i32_32x32x32_i8 v[84:99], v[202:205], v[148:151], v[84:99]
	ds_read_b128 v[202:205], v195
	v_mfma_i32_32x32x32_i8 v[84:99], v[206:209], v[152:155], v[84:99]
	ds_read_b128 v[206:209], v196
	v_mfma_i32_32x32x32_i8 v[84:99], v[210:213], v[156:159], v[84:99]
	ds_read_b128 v[210:213], v195 offset:2048
	v_mfma_i32_32x32x32_i8 v[84:99], v[214:217], v[160:163], v[84:99]
	ds_read_b128 v[214:217], v196 offset:2048
	v_readlane_b32 s50, v182, s43
	s_waitcnt lgkmcnt(6)
	v_mfma_f32_32x32x64_f8f6f4 v[2:17], v[100:107], v[116:123], v[2:17]
	ds_read_b128 v[218:221], v185 offset:32768
	ds_read_b128 v[222:225], v186 offset:32768
	ds_read_b128 v[242:245], v187 offset:32768
	ds_read_b128 v[246:249], v188 offset:32768
	v_mul_f32_e32 v82, s50, v168
	v_mul_f32_e32 v250, 0x3db8aa3b, v82
	v_fmamk_f32 v251, v250, 0xcb400000, v200
	s_add_i32 m0, s31, 32768
	v_fma_f32 v84, v84, v250, v251
	global_load_lds_dwordx4 v255, s[60:61]
	s_add_i32 m0, s31, 40960
	v_fma_f32 v85, v85, v250, v251
	global_load_lds_dwordx4 v201, s[60:61]
	v_fma_f32 v86, v86, v250, v251
	v_fma_f32 v87, v87, v250, v251
	v_exp_f32_e32 v84, v84
	v_exp_f32_e32 v85, v85
	v_exp_f32_e32 v86, v86
	v_exp_f32_e32 v87, v87
	v_fma_f32 v88, v88, v250, v251
	v_fma_f32 v89, v89, v250, v251
	v_fma_f32 v90, v90, v250, v251
	v_fma_f32 v91, v91, v250, v251
	s_waitcnt lgkmcnt(8)
	v_mfma_f32_32x32x64_f8f6f4 v[18:33], v[100:107], v[124:131], v[18:33]
	v_add_f32_e32 v67, v84, v85
	v_add_f32_e32 v68, v86, v87
	v_exp_f32_e32 v88, v88
	v_exp_f32_e32 v89, v89
	v_exp_f32_e32 v90, v90
	v_exp_f32_e32 v91, v91
	v_add_f32_e32 v67, v67, v68
	v_cvt_pk_fp8_f32 v108, v84, v85
	v_cvt_pk_fp8_f32 v108, v86, v87 op_sel:[0,0,1]
	v_fma_f32 v92, v92, v250, v251
	v_fma_f32 v93, v93, v250, v251
	v_fma_f32 v94, v94, v250, v251
	v_fma_f32 v95, v95, v250, v251
	v_add_f32_e32 v68, v88, v89
	v_add_f32_e32 v69, v90, v91
	s_waitcnt lgkmcnt(6)
	v_mfma_f32_32x32x64_f8f6f4 v[50:65], v[100:107], v[202:209], v[50:65]
	ds_read_b128 v[202:205], v189 offset:32768
	ds_read_b128 v[206:209], v190 offset:32768
	v_exp_f32_e32 v92, v92
	v_exp_f32_e32 v93, v93
	v_exp_f32_e32 v94, v94
	v_exp_f32_e32 v95, v95
	v_add_f32_e32 v68, v68, v69
	v_cvt_pk_fp8_f32 v109, v88, v89
	v_cvt_pk_fp8_f32 v109, v90, v91 op_sel:[0,0,1]
	v_fma_f32 v96, v96, v250, v251
	v_fma_f32 v97, v97, v250, v251
	v_fma_f32 v98, v98, v250, v251
	v_fma_f32 v99, v99, v250, v251
	v_add_f32_e32 v67, v67, v68
	v_add_f32_e32 v68, v92, v93
	v_add_f32_e32 v69, v94, v95
	s_waitcnt lgkmcnt(6)
	v_mfma_f32_32x32x64_f8f6f4 v[34:49], v[100:107], v[210:217], v[34:49]
	ds_read_b128 v[210:213], v191 offset:32768
	ds_read_b128 v[214:217], v192 offset:32768
	v_exp_f32_e32 v96, v96
	v_exp_f32_e32 v97, v97
	v_exp_f32_e32 v98, v98
	v_exp_f32_e32 v99, v99
	v_add_f32_e32 v68, v68, v69
	v_cvt_pk_fp8_f32 v110, v92, v93
	v_cvt_pk_fp8_f32 v110, v94, v95 op_sel:[0,0,1]
	v_add_f32_e32 v67, v67, v68
	v_add_f32_e32 v68, v96, v97
	v_add_f32_e32 v69, v98, v99
	s_add_u32 s60, s60, 0x4000
	s_addc_u32 s61, s61, 0
	v_add_f32_e32 v68, v68, v69
	v_cvt_pk_fp8_f32 v111, v96, v97
	v_cvt_pk_fp8_f32 v111, v98, v99 op_sel:[0,0,1]
	v_add_f32_e32 v67, v67, v68
	ds_write_b128 v194, v[108:111]
	v_cmp_ge_f32_e64 s[52:53], s42, v67
	v_add_f32_e32 v66, v66, v67
	s_add_i32 s43, s43, 1
	s_nop 0
	s_and_b64 s[54:55], s[54:55], s[52:53]
	s_waitcnt lgkmcnt(7)
	v_mfma_i32_32x32x32_i8 v[84:99], v[218:221], v[132:135], v[226:241]
	v_mfma_i32_32x32x32_i8 v[84:99], v[222:225], v[136:139], v[84:99]
	s_waitcnt vmcnt(2) lgkmcnt(0)
	s_barrier
.Lat_u4:
	ds_read_b128 v[112:115], v164
	v_mfma_i32_32x32x32_i8 v[84:99], v[242:245], v[140:143], v[84:99]
	ds_read_b128 v[116:119], v195 offset:22528
	ds_read_b128 v[120:123], v196 offset:22528
	s_add_i32 m0, s31, 65536
	ds_read_b128 v[124:127], v195 offset:20480
	global_load_lds_dwordx4 v252, s[60:61]
	s_add_i32 m0, s31, 73728
	v_mfma_i32_32x32x32_i8 v[84:99], v[246:249], v[144:147], v[84:99]
	global_load_lds_dwordx4 v254, s[60:61]
	ds_read_b128 v[128:131], v196 offset:20480
	v_mfma_i32_32x32x32_i8 v[84:99], v[202:205], v[148:151], v[84:99]
	ds_read_b128 v[202:205], v195 offset:16384
	v_mfma_i32_32x32x32_i8 v[84:99], v[206:209], v[152:155], v[84:99]
	ds_read_b128 v[206:209], v196 offset:16384
	v_mfma_i32_32x32x32_i8 v[84:99], v[210:213], v[156:159], v[84:99]
	ds_read_b128 v[210:213], v195 offset:18432
	v_mfma_i32_32x32x32_i8 v[84:99], v[214:217], v[160:163], v[84:99]
	ds_read_b128 v[214:217], v196 offset:18432
	v_readlane_b32 s50, v182, s43
	s_waitcnt lgkmcnt(6)
	v_mfma_f32_32x32x64_f8f6f4 v[2:17], v[108:115], v[116:123], v[2:17]
	ds_read_b128 v[218:221], v185
	ds_read_b128 v[222:225], v186
	ds_read_b128 v[242:245], v187
	ds_read_b128 v[246:249], v188
	v_mul_f32_e32 v82, s50, v168
	v_mul_f32_e32 v250, 0x3db8aa3b, v82
	v_fmamk_f32 v251, v250, 0xcb400000, v200
	s_mov_b32 m0, s31
	v_fma_f32 v84, v84, v250, v251
	global_load_lds_dwordx4 v255, s[60:61]
	s_add_i32 m0, s31, 8192
	v_fma_f32 v85, v85, v250, v251
	global_load_lds_dwordx4 v201, s[60:61]
	v_fma_f32 v86, v86, v250, v251
	v_fma_f32 v87, v87, v250, v251
	v_exp_f32_e32 v84, v84
	v_exp_f32_e32 v85, v85
	v_exp_f32_e32 v86, v86
	v_exp_f32_e32 v87, v87
	v_fma_f32 v88, v88, v250, v251
	v_fma_f32 v89, v89, v250, v251
	v_fma_f32 v90, v90, v250, v251
	v_fma_f32 v91, v91, v250, v251
	s_waitcnt lgkmcnt(8)
	v_mfma_f32_32x32x64_f8f6f4 v[18:33], v[108:115], v[124:131], v[18:33]
	v_add_f32_e32 v67, v84, v85
	v_add_f32_e32 v68, v86, v87
	v_exp_f32_e32 v88, v88
	v_exp_f32_e32 v89, v89
	v_exp_f32_e32 v90, v90
	v_exp_f32_e32 v91, v91
	v_add_f32_e32 v67, v67, v68
	v_cvt_pk_fp8_f32 v100, v84, v85
	v_cvt_pk_fp8_f32 v100, v86, v87 op_sel:[0,0,1]
	v_fma_f32 v92, v92, v250, v251
	v_fma_f32 v93, v93, v250, v251
	v_fma_f32 v94, v94, v250, v251
	v_fma_f32 v95, v95, v250, v251
	v_add_f32_e32 v68, v88, v89
	v_add_f32_e32 v69, v90, v91
	s_waitcnt lgkmcnt(6)
	v_mfma_f32_32x32x64_f8f6f4 v[50:65], v[108:115], v[202:209], v[50:65]
	ds_read_b128 v[202:205], v189
	ds_read_b128 v[206:209], v190
	v_exp_f32_e32 v92, v92
	v_exp_f32_e32 v93, v93
	v_exp_f32_e32 v94, v94
	v_exp_f32_e32 v95, v95
	v_add_f32_e32 v68, v68, v69
	v_cvt_pk_fp8_f32 v101, v88, v89
	v_cvt_pk_fp8_f32 v101, v90, v91 op_sel:[0,0,1]
	v_fma_f32 v96, v96, v250, v251
	v_fma_f32 v97, v97, v250, v251
	v_fma_f32 v98, v98, v250, v251
	v_fma_f32 v99, v99, v250, v251
	v_add_f32_e32 v67, v67, v68
	v_add_f32_e32 v68, v92, v93
	v_add_f32_e32 v69, v94, v95
	s_waitcnt lgkmcnt(6)
	v_mfma_f32_32x32x64_f8f6f4 v[34:49], v[108:115], v[210:217], v[34:49]
	ds_read_b128 v[210:213], v191
	ds_read_b128 v[214:217], v192
	v_exp_f32_e32 v96, v96
	v_exp_f32_e32 v97, v97
	v_exp_f32_e32 v98, v98
	v_exp_f32_e32 v99, v99
	v_add_f32_e32 v68, v68, v69
	v_cvt_pk_fp8_f32 v102, v92, v93
	v_cvt_pk_fp8_f32 v102, v94, v95 op_sel:[0,0,1]
	v_add_f32_e32 v67, v67, v68
	v_add_f32_e32 v68, v96, v97
	v_add_f32_e32 v69, v98, v99
	s_add_u32 s60, s60, 0x4000
	s_addc_u32 s61, s61, 0
	v_add_f32_e32 v68, v68, v69
	v_cvt_pk_fp8_f32 v103, v96, v97
	v_cvt_pk_fp8_f32 v103, v98, v99 op_sel:[0,0,1]
	v_add_f32_e32 v67, v67, v68
	ds_write_b128 v194, v[100:103] offset:8192
	v_cmp_ge_f32_e64 s[52:53], s42, v67
	v_add_f32_e32 v66, v66, v67
	s_add_i32 s43, s43, 1
	s_nop 0
	s_and_b64 s[54:55], s[54:55], s[52:53]
	s_waitcnt lgkmcnt(7)
	v_mfma_i32_32x32x32_i8 v[84:99], v[218:221], v[132:135], v[226:241]
	v_mfma_i32_32x32x32_i8 v[84:99], v[222:225], v[136:139], v[84:99]
	s_waitcnt vmcnt(2) lgkmcnt(0)
	s_barrier
.Lat_u5:
	ds_read_b128 v[104:107], v164 offset:8192
	v_mfma_i32_32x32x32_i8 v[84:99], v[242:245], v[140:143], v[84:99]
	ds_read_b128 v[116:119], v195 offset:38912
	ds_read_b128 v[120:123], v196 offset:38912
	s_cmp_gt_u32 s43, 29
	s_cbranch_scc1 .Lat_nok5
	s_add_i32 m0, s31, 81920
	ds_read_b128 v[124:127], v195 offset:36864
	global_load_lds_dwordx4 v252, s[60:61]
	s_add_i32 m0, s31, 90112
	v_mfma_i32_32x32x32_i8 v[84:99], v[246:249], v[144:147], v[84:99]
	global_load_lds_dwordx4 v254, s[60:61]
	s_branch .Lat_k5

.Lat_k5:
	ds_read_b128 v[128:131], v196 offset:36864
	v_mfma_i32_32x32x32_i8 v[84:99], v[202:205], v[148:151], v[84:99]
	ds_read_b128 v[202:205], v195 offset:32768
	v_mfma_i32_32x32x32_i8 v[84:99], v[206:209], v[152:155], v[84:99]
	ds_read_b128 v[206:209], v196 offset:32768
	v_mfma_i32_32x32x32_i8 v[84:99], v[210:213], v[156:159], v[84:99]
	ds_read_b128 v[210:213], v195 offset:34816
	v_mfma_i32_32x32x32_i8 v[84:99], v[214:217], v[160:163], v[84:99]
	ds_read_b128 v[214:217], v196 offset:34816
	v_readlane_b32 s50, v182, s43
	s_waitcnt lgkmcnt(6)
	v_mfma_f32_32x32x64_f8f6f4 v[2:17], v[100:107], v[116:123], v[2:17]
	ds_read_b128 v[218:221], v185 offset:16384
	ds_read_b128 v[222:225], v186 offset:16384
	ds_read_b128 v[242:245], v187 offset:16384
	ds_read_b128 v[246:249], v188 offset:16384
	v_mul_f32_e32 v82, s50, v168
	v_mul_f32_e32 v250, 0x3db8aa3b, v82
	v_fmamk_f32 v251, v250, 0xcb400000, v200
	s_add_i32 m0, s31, 16384
	v_fma_f32 v84, v84, v250, v251
	global_load_lds_dwordx4 v255, s[60:61]
	s_add_i32 m0, s31, 24576
	v_fma_f32 v85, v85, v250, v251
	global_load_lds_dwordx4 v201, s[60:61]
	v_fma_f32 v86, v86, v250, v251
	v_fma_f32 v87, v87, v250, v251
	v_exp_f32_e32 v84, v84
	v_exp_f32_e32 v85, v85
	v_exp_f32_e32 v86, v86
	v_exp_f32_e32 v87, v87
	v_fma_f32 v88, v88, v250, v251
	v_fma_f32 v89, v89, v250, v251
	v_fma_f32 v90, v90, v250, v251
	v_fma_f32 v91, v91, v250, v251
	s_waitcnt lgkmcnt(8)
	v_mfma_f32_32x32x64_f8f6f4 v[18:33], v[100:107], v[124:131], v[18:33]
	v_add_f32_e32 v67, v84, v85
	v_add_f32_e32 v68, v86, v87
	v_exp_f32_e32 v88, v88
	v_exp_f32_e32 v89, v89
	v_exp_f32_e32 v90, v90
	v_exp_f32_e32 v91, v91
	v_add_f32_e32 v67, v67, v68
	v_cvt_pk_fp8_f32 v108, v84, v85
	v_cvt_pk_fp8_f32 v108, v86, v87 op_sel:[0,0,1]
	v_fma_f32 v92, v92, v250, v251
	v_fma_f32 v93, v93, v250, v251
	v_fma_f32 v94, v94, v250, v251
	v_fma_f32 v95, v95, v250, v251
	v_add_f32_e32 v68, v88, v89
	v_add_f32_e32 v69, v90, v91
	s_waitcnt lgkmcnt(6)
	v_mfma_f32_32x32x64_f8f6f4 v[50:65], v[100:107], v[202:209], v[50:65]
	ds_read_b128 v[202:205], v189 offset:16384
	ds_read_b128 v[206:209], v190 offset:16384
	v_exp_f32_e32 v92, v92
	v_exp_f32_e32 v93, v93
	v_exp_f32_e32 v94, v94
	v_exp_f32_e32 v95, v95
	v_add_f32_e32 v68, v68, v69
	v_cvt_pk_fp8_f32 v109, v88, v89
	v_cvt_pk_fp8_f32 v109, v90, v91 op_sel:[0,0,1]
	v_fma_f32 v96, v96, v250, v251
	v_fma_f32 v97, v97, v250, v251
	v_fma_f32 v98, v98, v250, v251
	v_fma_f32 v99, v99, v250, v251
	v_add_f32_e32 v67, v67, v68
	v_add_f32_e32 v68, v92, v93
	v_add_f32_e32 v69, v94, v95
	s_waitcnt lgkmcnt(6)
	v_mfma_f32_32x32x64_f8f6f4 v[34:49], v[100:107], v[210:217], v[34:49]
	ds_read_b128 v[210:213], v191 offset:16384
	ds_read_b128 v[214:217], v192 offset:16384
	v_exp_f32_e32 v96, v96
	v_exp_f32_e32 v97, v97
	v_exp_f32_e32 v98, v98
	v_exp_f32_e32 v99, v99
	v_add_f32_e32 v68, v68, v69
	v_cvt_pk_fp8_f32 v110, v92, v93
	v_cvt_pk_fp8_f32 v110, v94, v95 op_sel:[0,0,1]
	v_add_f32_e32 v67, v67, v68
	v_add_f32_e32 v68, v96, v97
	v_add_f32_e32 v69, v98, v99
	s_add_u32 s60, s60, 0x4000
	s_addc_u32 s61, s61, 0
	v_add_f32_e32 v68, v68, v69
	v_cvt_pk_fp8_f32 v111, v96, v97
	v_cvt_pk_fp8_f32 v111, v98, v99 op_sel:[0,0,1]
	v_add_f32_e32 v67, v67, v68
	ds_write_b128 v194, v[108:111]
	v_cmp_ge_f32_e64 s[52:53], s42, v67
	v_add_f32_e32 v66, v66, v67
	s_add_i32 s43, s43, 1
	s_nop 0
	s_and_b64 s[54:55], s[54:55], s[52:53]
	s_waitcnt lgkmcnt(7)
	v_mfma_i32_32x32x32_i8 v[84:99], v[218:221], v[132:135], v[226:241]
	v_mfma_i32_32x32x32_i8 v[84:99], v[222:225], v[136:139], v[84:99]
	s_cmp_gt_u32 s43, 30
	s_cbranch_scc1 .Lat_drain
	s_waitcnt vmcnt(2) lgkmcnt(0)
	s_barrier
	s_branch .Lat_u0

.Lat_last:
	s_waitcnt vmcnt(0) lgkmcnt(0)
	s_barrier
	s_cmp_eq_u32 s34, 0
	s_cbranch_scc1 .Lat_nsw2
	v_swap_b32 v195, v196
.Lat_nsw2:
	s_cmp_lg_u64 s[54:55], exec
	s_cselect_b32 s1, 1, 0
	s_or_b32 s39, s39, s1
	v_add_u32_e32 v250, 0xc000, v184
	v_sub_u32_e32 v185, v185, v250
	v_sub_u32_e32 v186, v186, v250
	v_sub_u32_e32 v187, v187, v250
	v_sub_u32_e32 v188, v188, v250
	v_sub_u32_e32 v189, v189, v250
	v_sub_u32_e32 v190, v190, v250
	v_sub_u32_e32 v191, v191, v250
	v_sub_u32_e32 v192, v192, v250
